# attention item setup: FoX tile-skip metadata loads issued together (one wait instead of four), MoBA query-list entry loaded speculatively alongside the list count
# baseline (speedup 1.0000x reference)
.LBB0_799:
	s_add_i32 s13, s12, s2
	s_ashr_i32 s13, s13, 1
	s_lshl_b32 s14, s13, 2
	s_add_i32 s14, s14, 0
	s_add_i32 s14, s14, 0x21000
	v_mov_b32_e32 v1, s14
	ds_read_b32 v1, v1
	s_waitcnt lgkmcnt(0)
	v_readfirstlane_b32 s14, v1
	s_cmp_gt_i32 s14, s3
	s_cselect_b32 s12, s12, s13
	s_cselect_b32 s2, s13, s2
	s_sub_i32 s13, s2, s12
	s_cmp_gt_i32 s13, 1
	s_cbranch_scc1 .LBB0_799
	s_lshl_b32 s2, s12, 2
	s_add_i32 s2, s2, 0
	s_add_i32 s2, s2, 0x21000
	v_mov_b32_e32 v1, s2
	s_mul_hi_i32 s2, s12, 0x82082083
	s_add_i32 s2, s2, s12
	s_lshr_b32 s13, s2, 31
	s_ashr_i32 s2, s2, 5
	s_add_i32 s2, s2, s13
	s_mul_i32 s15, s2, 63
	s_sub_i32 s14, s12, s15
	s_lshl_b32 s12, s2, 6
	s_add_i32 s12, s12, s14
	s_ashr_i32 s13, s12, 31
	s_lshl_b64 s[12:13], s[12:13], 2
	s_add_u32 s12, s6, s12
	s_addc_u32 s13, s7, s13
	global_load_dword v3, v97, s[12:13]
	ds_read_b32 v1, v1
	s_ashr_i32 s22, s14, 31
	s_mul_hi_i32 s19, s2, 63
	s_add_u32 s18, s15, s14
	s_addc_u32 s19, s19, s22
	s_lshl_b64 s[18:19], s[18:19], 16
	s_add_u32 s18, s44, s18
	s_addc_u32 s19, s45, s19
	v_mov_b32_e32 v10, v0
	v_ashrrev_i32_e32 v11, 31, v0
	s_waitcnt lgkmcnt(0)
	v_sub_u32_e32 v1, s3, v1
	v_lshlrev_b32_e32 v2, 8, v1
	v_mov_b32_e32 v8, v2
	v_ashrrev_i32_e32 v9, 31, v2
	v_lshlrev_b64 v[8:9], 2, v[8:9]
	v_lshl_add_u64 v[8:9], s[18:19], 0, v[8:9]
	v_lshl_add_u64 v[8:9], v[10:11], 2, v[8:9]
	global_load_dword v12, v[8:9], off
	s_waitcnt vmcnt(0)
	v_sub_u32_e32 v1, v3, v2
	v_cmp_lt_i32_e32 vcc, v0, v1
	s_nop 1
	v_cndmask_b32_e32 v1, -1, v12, vcc
	v_max_i32_e32 v2, 0, v1
	v_lshrrev_b32_e32 v4, 2, v2
	v_and_b32_e32 v2, 0x3ffffffc, v2
	v_add_u32_e32 v2, s2, v2
	v_and_b32_e32 v3, 3, v1
	v_lshl_or_b32 v2, v2, 2, v3
	v_cmp_lt_i32_e32 vcc, -1, v1
	s_lshl_b32 s22, s14, 8
	s_mov_b64 s[12:13], 0
	v_cndmask_b32_e32 v6, -1, v2, vcc

.LBB0_812:
	s_ashr_i32 s3, s2, 31
	s_lshl_b64 s[12:13], s[2:3], 16
	s_add_u32 s12, s46, s12
	s_addc_u32 s13, s47, s13
	s_lshl_b32 s14, s26, 8
	s_lshl_b32 s3, s25, 11
	s_add_i32 s24, s27, -4
	s_and_b64 s[20:21], s[16:17], exec
	s_cselect_b32 s15, s24, s27
	v_cmp_gt_u32_e32 vcc, s15, v198
	s_mov_b64 s[22:23], 0
	s_and_saveexec_b64 s[20:21], vcc
	s_cbranch_execz .LBB0_814
	s_lshl_b32 s22, s2, 8
	s_ashr_i32 s23, s22, 31
	s_lshl_b64 s[22:23], s[22:23], 2
	s_add_u32 s15, s48, s22
	s_addc_u32 s52, s49, s23
	s_add_u32 s22, s15, 0x1000
	s_addc_u32 s23, s52, 0
	s_lshl_b32 s28, s26, 2
	s_ashr_i32 s29, s28, 31
	s_lshl_b64 s[28:29], s[28:29], 2
	s_add_u32 s50, s22, s28
	s_addc_u32 s51, s23, s29
	global_load_dwordx4 v[2:5], v97, s[50:51]
	s_add_u32 s28, s15, s28
	s_addc_u32 s29, s52, s29
	s_ashr_i32 s15, s14, 31
	global_load_dwordx4 v[8:11], v97, s[28:29]
	v_lshl_or_b32 v16, s25, 5, v198
	v_mov_b32_e32 v17, v97
	v_lshl_add_u64 v[16:17], v[16:17], 2, s[22:23]
	global_load_dword v12, v[16:17], off
	s_lshl_b64 s[22:23], s[14:15], 2
	s_add_u32 s22, s12, s22
	s_addc_u32 s23, s13, s23
	global_load_dword v14, v97, s[22:23]
	v_lshlrev_b32_e32 v18, 6, v198
	v_or_b32_e32 v18, s3, v18
	v_mov_b32_e32 v19, v97
	v_lshl_add_u64 v[18:19], v[18:19], 2, s[12:13]
	global_load_dword v13, v[18:19], off offset:252
	s_mov_b32 s15, 0xc2200000
	s_waitcnt vmcnt(0)
	v_max_f32_e32 v1, v5, v5
	v_max_f32_e32 v4, v4, v4
	v_max_f32_e32 v1, v4, v1
	v_max3_f32 v1, v2, v3, v1
	v_max_f32_e32 v5, v11, v11
	v_max_f32_e32 v4, v10, v10
	v_max_f32_e32 v4, v4, v5
	v_max3_f32 v4, v8, v9, v4
	v_mov_b32_e32 v5, v14
	v_mov_b32_e32 v3, v97
	v_add_f32_e32 v1, v1, v12
	v_sub_f32_e32 v2, v5, v13
	v_fmac_f32_e32 v2, v4, v1
	v_cmp_gt_f32_e32 vcc, s15, v2
	s_and_b64 s[22:23], vcc, exec
